# no acquire-invalidate at the barrier behind the prologue (no workspace line has been read before it)
# baseline (speedup 1.0000x reference)
; __device__ __forceinline__ unsigned xb_ld(unsigned* p)              { return __hip_atomic_load(p, __ATOMIC_RELAXED, __HIP_MEMORY_SCOPE_AGENT); }
; __device__ __forceinline__ unsigned xb_add(unsigned* p, unsigned v) { return __hip_atomic_fetch_add(p, v, __ATOMIC_RELAXED, __HIP_MEMORY_SCOPE_AGENT); }
; #define XB_SPIN(cond, bar) do { unsigned _sp = 0; while (cond) { __builtin_amdgcn_s_sleep(1); \
;     if ((++_sp & 255u) == 0u) { if (xb_ld(&(bar)[XB_TMO])) break; if (_sp > XB_SPIN_CAP) { atomicAdd(&(bar)[XB_TMO], 1u); break; } } } } while (0)
; __device__ __forceinline__ void xcd_barrier_impl(const XcdBarrier& b, bool leader) {
;     ...
;             const unsigned og = xb_add(&bar[XB_TOP], 1u);
;             const unsigned tg = og / nx;
;             if (og + 1u != (tg + 1u) * nx) XB_SPIN(xb_ld(&bar[XB_TOP]) < (tg + 1u) * nx, bar);
;             __builtin_amdgcn_fence(__ATOMIC_ACQUIRE, "agent");
;             asm volatile("s_waitcnt vmcnt(0)" ::: "memory");
;         } else {
;             XB_SPIN(xb_ld(&bar[XB_TOP]) < (gen + 1u) * nx, bar);
;             __builtin_amdgcn_fence(__ATOMIC_ACQUIRE, "agent");
;             asm volatile("s_waitcnt vmcnt(0)" ::: "memory");
.LBB0_191:
	s_or_b64 exec, exec, s[16:17]
	s_xor_b64 s[2:3], s[18:19], -1
	s_and_saveexec_b64 s[14:15], s[2:3]
	s_xor_b64 s[14:15], exec, s[14:15]
	s_cbranch_execz .LBB0_194
	s_mov_b64 s[14:15], exec
	v_mbcnt_lo_u32_b32 v0, s14, 0
	v_mbcnt_hi_u32_b32 v0, s15, v0
	v_cmp_eq_u32_e32 vcc, 0, v0
	s_and_b64 s[2:3], exec, vcc
	s_mov_b64 exec, s[2:3]
	s_cbranch_execz .LBB0_194
	s_bcnt1_i32_b64 s2, s[14:15]
	v_mov_b32_e32 v0, 0
	v_mov_b32_e32 v1, s2
	global_atomic_add v0, v1, s[12:13]
.LBB0_194:
	s_or_b64 exec, exec, s[10:11]
	s_waitcnt vmcnt(0)
	s_waitcnt vmcnt(0)
.LBB0_195:
	s_andn2_saveexec_b64 s[2:3], s[8:9]
	s_cbranch_execz .LBB0_212
	s_mov_b64 s[10:11], exec
	buffer_wbl2 sc1
	s_waitcnt lgkmcnt(0)
	s_waitcnt vmcnt(0)
	v_mbcnt_lo_u32_b32 v1, s10, 0
	s_add_u32 s8, s6, 0x7400
	v_mbcnt_hi_u32_b32 v1, s11, v1
	s_addc_u32 s9, s7, 0
	v_cmp_eq_u32_e32 vcc, 0, v1
	s_and_saveexec_b64 s[12:13], vcc
	s_cbranch_execz .LBB0_198
	s_bcnt1_i32_b64 s2, s[10:11]
	v_mov_b32_e32 v2, 0
	v_mov_b32_e32 v3, s2
	global_atomic_add v2, v2, v3, s[8:9] sc0

; __device__ __forceinline__ unsigned xb_ld(unsigned* p)              { return __hip_atomic_load(p, __ATOMIC_RELAXED, __HIP_MEMORY_SCOPE_AGENT); }
; __device__ __forceinline__ unsigned xb_add(unsigned* p, unsigned v) { return __hip_atomic_fetch_add(p, v, __ATOMIC_RELAXED, __HIP_MEMORY_SCOPE_AGENT); }
; #define XB_SPIN(cond, bar) do { unsigned _sp = 0; while (cond) { __builtin_amdgcn_s_sleep(1); \
;     if ((++_sp & 255u) == 0u) { if (xb_ld(&(bar)[XB_TMO])) break; if (_sp > XB_SPIN_CAP) { atomicAdd(&(bar)[XB_TMO], 1u); break; } } } } while (0)
; __device__ __forceinline__ void xcd_barrier_impl(const XcdBarrier& b, bool leader) {
;     ...
;             const unsigned og = xb_add(&bar[XB_TOP], 1u);
;             const unsigned tg = og / nx;
;             if (og + 1u != (tg + 1u) * nx) XB_SPIN(xb_ld(&bar[XB_TOP]) < (tg + 1u) * nx, bar);
;             __builtin_amdgcn_fence(__ATOMIC_ACQUIRE, "agent");
;             asm volatile("s_waitcnt vmcnt(0)" ::: "memory");
.LBB0_208:
	s_or_b64 exec, exec, s[12:13]
	s_xor_b64 s[2:3], s[14:15], -1
	s_and_saveexec_b64 s[8:9], s[2:3]
	s_xor_b64 s[8:9], exec, s[8:9]
	s_cbranch_execz .LBB0_211
	s_mov_b64 s[8:9], exec
	v_mbcnt_lo_u32_b32 v0, s8, 0
	v_mbcnt_hi_u32_b32 v0, s9, v0
	v_cmp_eq_u32_e32 vcc, 0, v0
	s_and_b64 s[2:3], exec, vcc
	s_mov_b64 exec, s[2:3]
	s_cbranch_execz .LBB0_211
	s_bcnt1_i32_b64 s2, s[8:9]
	v_mov_b32_e32 v0, 0
	v_mov_b32_e32 v1, s2
	global_atomic_add v0, v1, s[6:7]
.LBB0_211:
	s_or_b64 exec, exec, s[10:11]
	s_waitcnt vmcnt(0)
	s_waitcnt vmcnt(0)
; template <int I> __device__ __forceinline__ const float* karg_in() { return (const float*)(const GAS float*)karg_u64<I>(); }
; __device__ __forceinline__ unsigned char* karg_ws() { return (unsigned char*)(GAS unsigned char*)karg_u64<15>(); }
; __device__ __forceinline__ void xcd_barrier_impl(const XcdBarrier& b, bool leader) {
;     ...
;     __syncthreads();
; __global__ void __launch_bounds__(512, 2) trunk_fwd(Args args) {
;     ...
;     grid_barrier(wave_s);
; #pragma unroll 1
;     for (int layer = 0; layer < DEPTH; ++layer) {
;         const int li = layer >> 1;
;         if ((layer & 1) == 0) {
;             { unsigned char* ws = karg_ws();
;               pg8::Gemm g{(const bf16_t*)(ws + WS_XB), (const bf16_t*)(ws + WS_W_EIN + li * SZ_EIN), EIN, D, D, (const float*)(ws + WS_SSP)};
;               pg8::EpiEvenIn E{ws, karg_in<5>() + li * 64, karg_in<6>() + li * 64};
;     ...
;               for (int rep_ = 0; rep_ < REP_G1; ++rep_) run_gemm(g, E, wave_s);
.LBB0_212:
	s_or_b64 exec, exec, s[4:5]
	s_ashr_i32 s75, s74, 31
	s_lshr_b32 s2, s75, 29
	s_add_i32 s2, s74, s2
	s_and_b32 s3, s2, -8
	s_sub_i32 s16, s74, s3
	s_ashr_i32 s14, s2, 3
	s_cmpk_lt_i32 s74, 0x300
	s_cselect_b64 s[2:3], -1, 0
	s_lshr_b32 s0, s0, 8
	v_writelane_b32 v254, s2, 0
	s_lshl_b32 s12, s0, 14
	s_add_i32 s13, s12, 0
	v_writelane_b32 v254, s3, 1
	s_lshr_b32 s2, s16, 31
	s_or_b32 s2, s2, 0x60
	s_mul_i32 s2, s2, s16
	s_add_i32 s3, s2, s14
	s_mul_hi_i32 s4, s3, 0x2aaaaaab
	s_lshr_b32 s5, s4, 31
	s_ashr_i32 s4, s4, 4
	s_add_i32 s4, s4, s5
	s_lshl_b32 s5, s4, 3
	s_mulk_i32 s4, 0x60
	s_sub_i32 s4, s3, s4
	s_lshl_b32 s3, s1, 16
	v_writelane_b32 v254, s3, 2
	s_lshl_b32 s3, s0, 6
	v_writelane_b32 v254, s3, 3
	s_lshl_b32 s3, s1, 1
	s_or_b32 s3, s3, 1
	s_lshl_b32 s8, s3, 3
	s_lshl_b32 s11, s3, 14
	s_lshl_b32 s0, s1, 11
	s_lshl_b32 s3, s3, 10
	s_add_i32 s15, s13, s0
	v_writelane_b32 v254, s13, 4
	s_add_i32 s17, s3, s13
	s_add_i32 s13, 0, 0x2000
	s_add_i32 s12, s12, s13
	s_add_i32 s18, s12, s0
	s_add_i32 s3, s3, s12
	v_writelane_b32 v254, s15, 5
	s_add_i32 s12, s15, 0x8000
	v_writelane_b32 v254, s12, 6
	v_writelane_b32 v254, s17, 7
	s_add_i32 s12, s17, 0x8000
	v_writelane_b32 v254, s12, 8
	v_writelane_b32 v254, s18, 9
	s_add_i32 s12, s18, 0x8000
	v_writelane_b32 v254, s12, 10
	v_writelane_b32 v254, s3, 11
	s_add_i32 s3, s3, 0x8000
	v_writelane_b32 v254, s3, 12
	s_lshl_b32 s3, s1, 5
	v_writelane_b32 v254, s3, 13
	s_lshl_b32 s3, s78, 2
	s_add_i32 s3, s3, 0
	s_add_i32 s3, s3, 0x20000
	v_writelane_b32 v254, s3, 14
	s_lshl_b32 s3, s78, 12
	s_sub_i32 s6, 64, s5
	s_lshl_b32 s7, s1, 4
	s_lshl_b32 s9, s1, 15
	s_add_i32 s3, s3, 0
	s_min_u32 s6, s6, 8
	s_and_b32 s9, s9, 0x8000
	s_and_b32 s10, s7, 32
	s_and_b32 s11, s11, 0xc000
	v_writelane_b32 v254, s3, 15
	s_add_i32 s3, s3, 0x18000
	s_cmpk_lt_i32 s74, 0x100
	v_writelane_b32 v254, s3, 16
	s_cselect_b64 s[18:19], -1, 0
	s_lshl_b32 s3, s16, 6
	s_sub_i32 s2, s2, s3
	s_add_i32 s2, s2, s14
	s_ashr_i32 s3, s2, 31
	s_lshr_b32 s3, s3, 27
	s_add_i32 s3, s2, s3
	v_writelane_b32 v254, s18, 17
	s_ashr_i32 s12, s3, 5
	s_lshl_b32 s12, s12, 3
	v_writelane_b32 v254, s19, 18
	v_writelane_b32 v254, s14, 19
	s_sub_i32 s14, 64, s12
	s_andn2_b32 s3, s3, 31
	s_min_u32 s14, s14, 8
	s_sub_i32 s15, s2, s3
	s_cmpk_lt_i32 s74, 0x1c0
	s_mul_i32 s3, s16, 24
	s_cselect_b64 s[18:19], -1, 0
	s_add_i32 s2, s2, s3
	v_writelane_b32 v254, s18, 20
	s_mul_hi_i32 s3, s2, 0x92492493
	s_add_i32 s3, s3, s2
	v_writelane_b32 v254, s19, 21
	v_writelane_b32 v254, s16, 22
	s_lshr_b32 s16, s3, 31
	s_ashr_i32 s3, s3, 5
	s_add_i32 s3, s3, s16
	s_lshl_b32 s16, s3, 3
	s_mul_i32 s3, s3, 56
	s_lshl_b32 s19, s78, 3
	s_sub_i32 s18, s2, s3
	s_and_b32 s2, s19, 0x1fffffe0
	v_writelane_b32 v254, s2, 23
	s_lshl_b32 s1, s1, 6
	v_writelane_b32 v254, s1, 24
	s_lshl_b32 s1, s78, 8
	s_add_i32 s1, s1, 0
	s_add_i32 s1, s1, 0x14000
	v_writelane_b32 v254, s1, 25
	s_lshl_b32 s1, s78, 10
	s_add_i32 s2, s1, 0
	v_writelane_b32 v254, s2, 26
	s_add_i32 s3, s2, 0x6000
	v_writelane_b32 v254, s3, 27
	s_add_i32 s2, s2, 0x8000
	v_writelane_b32 v254, s2, 28
	s_sext_i32_i8 s2, s4
	s_waitcnt vmcnt(15)
	v_cvt_f32_ubyte0_e32 v1, s6
	s_waitcnt lgkmcnt(0)
	v_cvt_f32_i32_e32 v0, s2
	v_rcp_iflag_f32_e32 v2, v1
	s_add_i32 s1, s1, s13
	s_sub_i32 s17, 64, s16
	v_writelane_b32 v254, s1, 29
	v_mul_f32_e32 v2, v0, v2
	v_trunc_f32_e32 v2, v2
	v_fma_f32 v0, -v2, v1, v0
	v_cvt_i32_f32_e32 v2, v2
	s_ashr_i32 s1, s2, 30
	s_min_u32 s17, s17, 8
	s_or_b32 s1, s1, 1
	v_cmp_ge_f32_e64 s[2:3], |v0|, v1
	s_and_b64 s[2:3], s[2:3], exec
	s_cselect_b32 s1, s1, 0
	v_readfirstlane_b32 s2, v2
	s_add_i32 s2, s2, s1
	s_sext_i32_i8 s1, s2
	v_writelane_b32 v254, s1, 30
	s_mul_i32 s1, s2, s6
	s_sub_i32 s1, s4, s1
	s_sext_i32_i8 s1, s1
	s_add_i32 s20, s5, s1
	s_sext_i32_i8 s1, s15
	v_cvt_f32_ubyte0_e32 v1, s14
	v_cvt_f32_i32_e32 v0, s1
	v_rcp_iflag_f32_e32 v2, v1
	s_mov_b32 s4, s20
	s_ashr_i32 s21, s20, 31
	v_writelane_b32 v254, s4, 31
	v_mul_f32_e32 v2, v0, v2
	s_bfe_i64 s[2:3], s[2:3], 0x80000
	v_writelane_b32 v254, s5, 32
	s_lshl_b64 s[4:5], s[20:21], 18
	v_writelane_b32 v254, s4, 33
	v_trunc_f32_e32 v2, v2
	s_lshl_b64 s[2:3], s[2:3], 18
	v_writelane_b32 v254, s5, 34
	v_fma_f32 v0, -v2, v1, v0
	v_cvt_i32_f32_e32 v2, v2
	v_writelane_b32 v254, s2, 35
	s_ashr_i32 s1, s1, 30
	s_or_b32 s1, s1, 1
	v_writelane_b32 v254, s3, 36
	v_cmp_ge_f32_e64 s[2:3], |v0|, v1
	s_and_b64 s[2:3], s[2:3], exec
	s_cselect_b32 s1, s1, 0
	v_readfirstlane_b32 s2, v2
	s_add_i32 s1, s2, s1
	s_mul_i32 s2, s1, s14
	s_sub_i32 s2, s15, s2
	s_sext_i32_i8 s2, s2
	s_add_i32 s2, s12, s2
	v_writelane_b32 v254, s2, 37
	s_sext_i32_i8 s2, s18
	v_cvt_f32_ubyte0_e32 v1, s17
	v_cvt_f32_i32_e32 v0, s2
	v_rcp_iflag_f32_e32 v2, v1
	s_sext_i32_i8 s1, s1
	v_writelane_b32 v254, s1, 38
	s_ashr_i32 s1, s2, 30
	v_mul_f32_e32 v2, v0, v2
	v_trunc_f32_e32 v2, v2
	v_fma_f32 v0, -v2, v1, v0
	v_cvt_i32_f32_e32 v2, v2
	s_or_b32 s1, s1, 1
	v_cmp_ge_f32_e64 s[2:3], |v0|, v1
	s_and_b64 s[2:3], s[2:3], exec
	s_cselect_b32 s1, s1, 0
	v_readfirstlane_b32 s2, v2
	s_add_i32 s1, s2, s1
	s_sext_i32_i8 s2, s1
	s_mul_i32 s1, s1, s17
	s_sub_i32 s1, s18, s1
	s_sext_i32_i8 s1, s1
	v_writelane_b32 v254, s2, 39
	s_add_i32 s1, s16, s1
	v_writelane_b32 v254, s1, 40
	s_abs_i32 s1, s74
	v_writelane_b32 v254, s1, 41
	s_add_i32 s1, 0, 0x20960
	v_writelane_b32 v254, s1, 42
	s_add_i32 s1, 0, 0x20964
	v_writelane_b32 v254, s1, 43
	s_lshl_b32 s1, s7, 1
	v_writelane_b32 v254, s1, 44
	s_lshl_b32 s1, s8, 1
	v_writelane_b32 v254, s1, 45
	s_lshl_b32 s1, s9, 1
	v_writelane_b32 v254, s1, 46
	s_lshl_b32 s1, s10, 1
	v_writelane_b32 v254, s1, 47
	s_lshl_b32 s1, s11, 1
	v_writelane_b32 v254, s1, 48
	s_add_i32 s1, 0, 0x20010
	v_writelane_b32 v254, s1, 49
	s_add_i32 s1, 0, 0x19400
	v_writelane_b32 v254, s1, 50
	s_lshl_b32 s1, s19, 1
	v_writelane_b32 v254, s1, 51
	s_lshl_b32 s0, s0, 1
	v_writelane_b32 v254, s0, 52
	s_add_i32 s0, 0, 0x200
	v_writelane_b32 v254, s0, 53
	s_add_i32 s0, 0, 0xc200
	v_writelane_b32 v254, s0, 54
	s_mov_b32 s1, 0
	v_writelane_b32 v254, s0, 55
	v_mov_b32_e32 v1, 0
	s_mov_b32 s95, 0x20000
	v_writelane_b32 v254, s1, 56
	v_writelane_b32 v254, s74, 57
	s_mov_b32 s67, 0x42fe0000
	s_mov_b32 s68, 0x40c0c00
	v_writelane_b32 v254, s75, 58
	v_writelane_b32 v254, s76, 59
	v_mov_b32_e32 v228, 0x358637bd
	s_mov_b32 s84, 0x800000
	v_writelane_b32 v254, s77, 60
	v_writelane_b32 v254, s78, 61
	v_writelane_b32 v254, s79, 62
	v_writelane_b32 v254, s80, 63
	s_movk_i32 s86, 0xff
	s_movk_i32 s87, 0xc0
	v_writelane_b32 v255, s81, 0
	v_writelane_b32 v255, s82, 1
	v_mov_b32_e32 v229, 1
	s_brev_b32 s94, -2
	v_bfrev_b32_e32 v230, 1
	v_mov_b32_e32 v231, 0xff800000
	v_mov_b64_e32 v[202:203], 0x100
	v_mov_b64_e32 v[204:205], 0xff
	v_mov_b32_e32 v240, v1
	v_mov_b32_e32 v241, v1
	v_mov_b32_e32 v242, v1
	v_mov_b32_e32 v243, v1
	v_mov_b32_e32 v232, 0x9f
	v_mov_b32_e32 v233, 0x446
	s_movk_i32 s88, 0x3a8
	s_movk_i32 s89, 0xff60
	s_movk_i32 s92, 0xfc58
	s_brev_b32 s85, 1
	s_movk_i32 s93, 0xf00
	s_mov_b32 s54, 0
	s_mov_b64 s[90:91], 0x80
	v_writelane_b32 v255, s83, 2
	s_barrier
	s_branch .LBB0_216
